# expert-major order variant: inside an expert block row-tile-major (pn = u and 7, rt = u >> 3): the 8 column tiles of a row tile adjacent
# baseline (speedup 1.0000x reference)
.LBB0_717:
	s_cmp_lt_i32 s76, s43
	s_cselect_b32 s45, s76, s44
	s_cmp_lt_i32 s45, 0
	s_cbranch_scc1 .LBB0_741
	s_add_u32 s8, s10, 0x1cd90000
	s_addc_u32 s9, s11, 0
	s_add_u32 s46, s10, 0x3adc0000
	s_addc_u32 s47, s11, 0
	s_abs_i32 s48, s42
	v_cvt_f32_u32_e32 v1, s48
	s_sub_i32 s2, 0, s48
	s_abs_i32 s1, s45
	s_ashr_i32 s0, s45, 31
	v_rcp_iflag_f32_e32 v1, v1
	s_ashr_i32 s49, s42, 31
	s_lshr_b32 s5, s4, 6
	s_xor_b32 s0, s0, s49
	v_mul_f32_e32 v1, 0x4f7ffffe, v1
	v_cvt_u32_f32_e32 v1, v1
	v_bfe_u32 v3, v0, 2, 4
	v_lshrrev_b32_e32 v4, 3, v0
	s_movk_i32 s61, 0x81
	v_readfirstlane_b32 s50, v1
	s_mul_i32 s2, s2, s50
	s_mul_hi_u32 s2, s50, s2
	s_add_i32 s50, s50, s2
	s_lshr_b32 s89, s45, 3
	s_lshl_b32 s89, s89, 2
	s_add_i32 s89, s89, 0x202e0
	v_mov_b32_e32 v222, s89
	ds_read_b32 v222, v222
	s_waitcnt lgkmcnt(0)
	v_lshlrev_b32_e32 v222, 2, v222
	v_add_u32_e32 v222, 0x20240, v222
	ds_read2_b32 v[252:253], v222 offset1:1
	s_waitcnt lgkmcnt(0)
	v_readfirstlane_b32 s90, v252
	v_readfirstlane_b32 s91, v253
	s_nop 3
	s_sub_i32 s91, s91, s90
	s_lshl_b32 s92, s90, 3
	s_sub_i32 s92, s45, s92
	s_and_b32 s18, s92, 7
	s_lshr_b32 s92, s92, 3
	s_add_i32 s12, s90, s92
	s_lshl_b32 s0, s12, 2
	s_add_i32 s0, s0, 0
	s_add_i32 s0, s0, 0x202e0
	v_mov_b32_e32 v1, s0
	ds_read_b32 v5, v1
	v_and_or_b32 v1, v4, 48, v3
	v_or_b32_e32 v4, 64, v4
	s_movk_i32 s0, 0x70
	v_and_or_b32 v186, v4, s0, v3
	s_waitcnt lgkmcnt(0)
	v_lshlrev_b32_e32 v3, 2, v5
	v_add_u32_e32 v3, 0, v3
	v_add_u32_e32 v4, 0x20240, v3
	ds_read_b32 v4, v4
	v_add_u32_e32 v3, 0x201c0, v3
	ds_read_b32 v3, v3
	v_readfirstlane_b32 s2, v5
	s_ashr_i32 s3, s2, 31
	s_waitcnt lgkmcnt(1)
	v_sub_u32_e32 v4, s12, v4
	v_lshlrev_b32_e32 v18, 8, v4
	v_lshlrev_b32_e32 v4, 6, v5
	s_waitcnt lgkmcnt(0)
	v_add_u32_e32 v19, -1, v3
	v_add_u32_e32 v4, 0, v4
	v_or_b32_e32 v22, v18, v1
	v_add_u32_e32 v20, 0x208e0, v4
	v_min_i32_e32 v22, v22, v19
	ds_read2_b32 v[4:5], v20 offset0:1 offset1:2
	ds_read2_b32 v[6:7], v20 offset0:3 offset1:4
	ds_read2_b32 v[8:9], v20 offset0:5 offset1:6
	ds_read2_b32 v[10:11], v20 offset0:7 offset1:8
	ds_read2_b32 v[12:13], v20 offset0:9 offset1:10
	ds_read2_b32 v[14:15], v20 offset0:11 offset1:12
	ds_read2_b32 v[16:17], v20 offset0:13 offset1:14
	ds_read_b32 v21, v20 offset:60
	s_waitcnt lgkmcnt(7)
	v_cmp_ge_i32_e32 vcc, v22, v4
	v_or_b32_e32 v25, v18, v186
	v_min_i32_e32 v25, v25, v19
	v_cndmask_b32_e64 v23, 0, 1, vcc
	v_cmp_ge_i32_e32 vcc, v22, v5
	v_or_b32_e32 v28, 0x80, v18
	v_or_b32_e32 v29, v28, v1
	v_cndmask_b32_e64 v24, 0, 1, vcc
	s_waitcnt lgkmcnt(6)
	v_cmp_ge_i32_e32 vcc, v22, v6
	v_min_i32_e32 v29, v29, v19
	v_or_b32_e32 v28, v28, v186
	v_addc_co_u32_e32 v23, vcc, v23, v24, vcc
	v_cmp_ge_i32_e32 vcc, v22, v7
	v_min_i32_e32 v19, v28, v19
	s_lshl_b64 s[0:1], s[2:3], 15
	v_cndmask_b32_e64 v24, 0, 1, vcc
	s_waitcnt lgkmcnt(5)
	v_cmp_ge_i32_e32 vcc, v22, v8
	s_add_u32 s0, s46, s0
	s_addc_u32 s1, s47, s1
	v_addc_co_u32_e32 v23, vcc, v23, v24, vcc
	v_cmp_ge_i32_e32 vcc, v22, v9
	v_sub_u32_e32 v3, v3, v18
	s_nop 0
	v_cndmask_b32_e64 v24, 0, 1, vcc
	s_waitcnt lgkmcnt(4)
	v_cmp_ge_i32_e32 vcc, v22, v10
	s_nop 1
	v_addc_co_u32_e32 v23, vcc, v23, v24, vcc
	v_cmp_ge_i32_e32 vcc, v22, v11
	s_nop 1
	v_cndmask_b32_e64 v24, 0, 1, vcc
	s_waitcnt lgkmcnt(3)
	v_cmp_ge_i32_e32 vcc, v22, v12
	s_nop 1
	v_addc_co_u32_e32 v23, vcc, v23, v24, vcc
	v_cmp_ge_i32_e32 vcc, v22, v13
	s_nop 1
	v_cndmask_b32_e64 v24, 0, 1, vcc
	s_waitcnt lgkmcnt(2)
	v_cmp_ge_i32_e32 vcc, v22, v14
	s_nop 1
	v_addc_co_u32_e32 v23, vcc, v23, v24, vcc
	v_cmp_ge_i32_e32 vcc, v22, v15
	s_nop 1
	v_cndmask_b32_e64 v24, 0, 1, vcc
	s_waitcnt lgkmcnt(1)
	v_cmp_ge_i32_e32 vcc, v22, v16
	s_nop 1
	v_addc_co_u32_e32 v23, vcc, v23, v24, vcc
	v_cmp_ge_i32_e32 vcc, v22, v17
	s_nop 1
	v_cndmask_b32_e64 v24, 0, 1, vcc
	s_waitcnt lgkmcnt(0)
	v_cmp_ge_i32_e32 vcc, v22, v21
	s_nop 1
	v_addc_co_u32_e32 v23, vcc, v23, v24, vcc
	v_cmp_ge_i32_e32 vcc, v25, v4
	v_lshl_add_u32 v24, v23, 2, v20
	ds_read_b32 v24, v24
	v_cndmask_b32_e64 v26, 0, 1, vcc
	v_cmp_ge_i32_e32 vcc, v25, v5
	s_nop 1
	v_cndmask_b32_e64 v27, 0, 1, vcc
	v_cmp_ge_i32_e32 vcc, v25, v6
	s_nop 1
	v_addc_co_u32_e32 v26, vcc, v26, v27, vcc
	v_cmp_ge_i32_e32 vcc, v25, v7
	s_nop 1
	v_cndmask_b32_e64 v27, 0, 1, vcc
	v_cmp_ge_i32_e32 vcc, v25, v8
	s_nop 1
	v_addc_co_u32_e32 v26, vcc, v26, v27, vcc
	v_cmp_ge_i32_e32 vcc, v25, v9
	s_nop 1
	v_cndmask_b32_e64 v27, 0, 1, vcc
	v_cmp_ge_i32_e32 vcc, v25, v10
	s_nop 1
	v_addc_co_u32_e32 v26, vcc, v26, v27, vcc
	v_cmp_ge_i32_e32 vcc, v25, v11
	s_nop 1
	v_cndmask_b32_e64 v27, 0, 1, vcc
	v_cmp_ge_i32_e32 vcc, v25, v12
	s_nop 1
	v_addc_co_u32_e32 v26, vcc, v26, v27, vcc
	v_cmp_ge_i32_e32 vcc, v25, v13
	s_nop 1
	v_cndmask_b32_e64 v27, 0, 1, vcc
	v_cmp_ge_i32_e32 vcc, v25, v14
	s_nop 1
	v_addc_co_u32_e32 v26, vcc, v26, v27, vcc
	v_cmp_ge_i32_e32 vcc, v25, v15
	s_nop 1
	v_cndmask_b32_e64 v27, 0, 1, vcc
	v_cmp_ge_i32_e32 vcc, v25, v16
	s_nop 1
	v_addc_co_u32_e32 v26, vcc, v26, v27, vcc
	v_cmp_ge_i32_e32 vcc, v25, v17
	s_nop 1
	v_cndmask_b32_e64 v27, 0, 1, vcc
	v_cmp_ge_i32_e32 vcc, v25, v21
	s_nop 1
	v_addc_co_u32_e32 v26, vcc, v26, v27, vcc
	v_cmp_ge_i32_e32 vcc, v29, v4
	v_lshl_add_u32 v27, v26, 2, v20
	s_nop 0
	v_cndmask_b32_e64 v30, 0, 1, vcc
	v_cmp_ge_i32_e32 vcc, v29, v5
	s_nop 1
	v_cndmask_b32_e64 v31, 0, 1, vcc
	v_cmp_ge_i32_e32 vcc, v29, v6
	s_nop 1
	v_addc_co_u32_e32 v30, vcc, v30, v31, vcc
	v_cmp_ge_i32_e32 vcc, v29, v7
	s_nop 1
	v_cndmask_b32_e64 v31, 0, 1, vcc
	v_cmp_ge_i32_e32 vcc, v29, v8
	s_nop 1
	v_addc_co_u32_e32 v30, vcc, v30, v31, vcc
	v_cmp_ge_i32_e32 vcc, v29, v9
	s_nop 1
	v_cndmask_b32_e64 v31, 0, 1, vcc
	v_cmp_ge_i32_e32 vcc, v29, v10
	s_nop 1
	v_addc_co_u32_e32 v30, vcc, v30, v31, vcc
	v_cmp_ge_i32_e32 vcc, v29, v11
	s_nop 1
	v_cndmask_b32_e64 v31, 0, 1, vcc
	v_cmp_ge_i32_e32 vcc, v29, v12
	s_nop 1
	v_addc_co_u32_e32 v30, vcc, v30, v31, vcc
	v_cmp_ge_i32_e32 vcc, v29, v13
	s_nop 1
	v_cndmask_b32_e64 v31, 0, 1, vcc
	v_cmp_ge_i32_e32 vcc, v29, v14
	s_nop 1
	v_addc_co_u32_e32 v30, vcc, v30, v31, vcc
	v_cmp_ge_i32_e32 vcc, v29, v15
	s_nop 1
	v_cndmask_b32_e64 v31, 0, 1, vcc
	v_cmp_ge_i32_e32 vcc, v29, v16
	s_nop 1
	v_addc_co_u32_e32 v30, vcc, v30, v31, vcc
	v_cmp_ge_i32_e32 vcc, v29, v17
	s_nop 1
	v_cndmask_b32_e64 v31, 0, 1, vcc
	v_cmp_ge_i32_e32 vcc, v29, v21
	s_nop 1
	v_addc_co_u32_e32 v30, vcc, v30, v31, vcc
	v_cmp_ge_i32_e32 vcc, v19, v4
	v_lshl_add_u32 v31, v30, 2, v20
	s_nop 0
	v_cndmask_b32_e64 v4, 0, 1, vcc
	v_cmp_ge_i32_e32 vcc, v19, v5
	s_nop 1
	v_cndmask_b32_e64 v5, 0, 1, vcc
	v_cmp_ge_i32_e32 vcc, v19, v6
	s_nop 1
	v_addc_co_u32_e32 v4, vcc, v4, v5, vcc
	v_cmp_ge_i32_e32 vcc, v19, v7
	s_nop 1
	v_cndmask_b32_e64 v5, 0, 1, vcc
	v_cmp_ge_i32_e32 vcc, v19, v8
	s_nop 1
	v_addc_co_u32_e32 v4, vcc, v4, v5, vcc
	v_cmp_ge_i32_e32 vcc, v19, v9
	s_nop 1
	v_cndmask_b32_e64 v5, 0, 1, vcc
	v_cmp_ge_i32_e32 vcc, v19, v10
	s_nop 1
	v_addc_co_u32_e32 v4, vcc, v4, v5, vcc
	v_cmp_ge_i32_e32 vcc, v19, v11
	s_nop 1
	v_cndmask_b32_e64 v5, 0, 1, vcc
	v_cmp_ge_i32_e32 vcc, v19, v12
	s_nop 1
	v_addc_co_u32_e32 v4, vcc, v4, v5, vcc
	v_cmp_ge_i32_e32 vcc, v19, v13
	s_nop 1
	v_cndmask_b32_e64 v5, 0, 1, vcc
	v_cmp_ge_i32_e32 vcc, v19, v14
	s_nop 1
	v_addc_co_u32_e32 v4, vcc, v4, v5, vcc
	v_cmp_ge_i32_e32 vcc, v19, v15
	s_nop 1
	v_cndmask_b32_e64 v5, 0, 1, vcc
	v_cmp_ge_i32_e32 vcc, v19, v16
	s_nop 1
	v_addc_co_u32_e32 v4, vcc, v4, v5, vcc
	v_cmp_ge_i32_e32 vcc, v19, v17
	s_nop 1
	v_cndmask_b32_e64 v5, 0, 1, vcc
	v_cmp_ge_i32_e32 vcc, v19, v21
	s_nop 1
	v_addc_co_u32_e32 v8, vcc, v4, v5, vcc
	v_lshl_add_u32 v4, v8, 2, v20
	ds_read_b32 v6, v27
	ds_read_b32 v9, v31
	ds_read_b32 v10, v4
	s_waitcnt lgkmcnt(3)
	v_sub_u32_e32 v4, v22, v24
	v_lshl_add_u32 v4, v23, 9, v4
	s_waitcnt lgkmcnt(2)
	v_sub_u32_e32 v6, v25, v6
	v_ashrrev_i32_e32 v5, 31, v4
	v_lshl_add_u32 v6, v26, 9, v6
	v_lshl_add_u64 v[4:5], v[4:5], 2, s[0:1]
	v_ashrrev_i32_e32 v7, 31, v6
	v_lshl_add_u64 v[6:7], v[6:7], 2, s[0:1]
	global_load_dword v11, v[4:5], off
	global_load_dword v12, v[6:7], off
	v_lshlrev_b32_e32 v4, 4, v0
	v_and_b32_e32 v5, 32, v0
	v_bitop3_b32 v4, v4, v5, 48 bitop3:0x6c
	v_and_or_b32 v187, v0, 64, v4
	s_waitcnt lgkmcnt(1)
	v_sub_u32_e32 v4, v29, v9
	v_lshl_add_u32 v6, v8, 9, v19
	v_lshl_add_u32 v4, v30, 9, v4
	s_waitcnt lgkmcnt(0)
	v_sub_u32_e32 v6, v6, v10
	v_ashrrev_i32_e32 v5, 31, v4
	v_ashrrev_i32_e32 v7, 31, v6
	v_lshl_add_u64 v[4:5], v[4:5], 2, s[0:1]
	v_lshl_add_u64 v[6:7], v[6:7], 2, s[0:1]
	s_lshl_b32 s0, s5, 10
	global_load_dword v8, v[4:5], off
	global_load_dword v9, v[6:7], off
	s_waitcnt vmcnt(0)
	s_add_i32 s51, s0, 0
	s_waitcnt lgkmcnt(0)
	s_barrier
	s_mov_b32 m0, s51
	s_add_i32 s60, s51, 0x2000
	v_cmp_gt_i32_e64 s[0:1], s61, v3
	s_and_b64 vcc, exec, s[0:1]
	s_waitcnt vmcnt(3)
	v_lshl_or_b32 v178, v11, 12, v187
	s_waitcnt vmcnt(2)
	v_lshl_or_b32 v180, v12, 12, v187
	global_load_lds_dwordx4 v178, s[8:9]
	s_mov_b32 m0, s60
	s_waitcnt vmcnt(0)
	v_lshl_or_b32 v182, v8, 12, v187
	global_load_lds_dwordx4 v180, s[8:9]
	v_lshl_or_b32 v184, v9, 12, v187
	s_cbranch_vccnz .LBB0_720
	s_add_i32 m0, s51, 0x4000
	s_nop 0
	global_load_lds_dwordx4 v182, s[8:9]
	s_add_i32 m0, s51, 0x6000
	s_nop 0
	global_load_lds_dwordx4 v184, s[8:9]

.LBB0_721:
	s_add_i32 s0, s45, s33
	s_cmp_lt_i32 s45, s43
	s_cselect_b32 s1, s44, -1
	s_cmp_lt_i32 s0, s43
	s_cselect_b32 s45, s0, s1
	s_cmp_lt_i32 s45, 0
	s_cselect_b64 s[14:15], -1, 0
	s_and_b64 vcc, exec, s[14:15]
	v_mov_b32_e32 v209, v178
	v_mov_b32_e32 v210, v180
	v_mov_b32_e32 v211, v182
	v_mov_b32_e32 v212, v184
	s_mov_b32 s16, s18
	s_cbranch_vccnz .LBB0_723
	s_lshr_b32 s89, s45, 3
	s_lshl_b32 s89, s89, 2
	s_add_i32 s89, s89, 0x202e0
	v_mov_b32_e32 v222, s89
	ds_read_b32 v222, v222
	s_waitcnt lgkmcnt(0)
	v_lshlrev_b32_e32 v222, 2, v222
	v_add_u32_e32 v222, 0x20240, v222
	ds_read2_b32 v[252:253], v222 offset1:1
	s_waitcnt lgkmcnt(0)
	v_readfirstlane_b32 s90, v252
	v_readfirstlane_b32 s91, v253
	s_nop 3
	s_sub_i32 s91, s91, s90
	s_lshl_b32 s92, s90, 3
	s_sub_i32 s92, s45, s92
	s_and_b32 s16, s92, 7
	s_lshr_b32 s92, s92, 3
	s_add_i32 s4, s90, s92
	s_lshl_b32 s0, s4, 2
	s_add_i32 s0, s0, 0
	s_add_i32 s0, s0, 0x202e0
	v_mov_b32_e32 v30, s0
	ds_read_b32 v30, v30
	s_ashr_i32 s17, s16, 31
	s_waitcnt lgkmcnt(0)
	v_lshlrev_b32_e32 v31, 2, v30
	v_add_u32_e32 v31, 0, v31
	v_add_u32_e32 v32, 0x20240, v31
	ds_read_b32 v32, v32
	v_add_u32_e32 v31, 0x201c0, v31
	ds_read_b32 v48, v31
	v_readfirstlane_b32 s2, v30
	v_lshlrev_b32_e32 v30, 6, v30
	s_waitcnt lgkmcnt(0)
	v_sub_u32_e32 v31, s4, v32
	v_lshlrev_b32_e32 v49, 8, v31
	v_add_u32_e32 v50, -1, v48
	v_add_u32_e32 v30, 0, v30
	v_or_b32_e32 v53, v49, v1
	v_add_u32_e32 v51, 0x208e0, v30
	v_min_i32_e32 v53, v53, v50
	ds_read2_b32 v[30:31], v51 offset0:1 offset1:2
	ds_read2_b32 v[32:33], v51 offset0:3 offset1:4
	ds_read2_b32 v[38:39], v51 offset0:5 offset1:6
	ds_read2_b32 v[40:41], v51 offset0:7 offset1:8
	ds_read2_b32 v[42:43], v51 offset0:9 offset1:10
	ds_read2_b32 v[44:45], v51 offset0:11 offset1:12
	ds_read2_b32 v[46:47], v51 offset0:13 offset1:14
	ds_read_b32 v52, v51 offset:60
	s_waitcnt lgkmcnt(0)
	v_cmp_ge_i32_e32 vcc, v53, v30
	v_or_b32_e32 v56, v49, v186
	v_min_i32_e32 v56, v56, v50
	v_cndmask_b32_e64 v54, 0, 1, vcc
	v_cmp_ge_i32_e32 vcc, v53, v31
	v_or_b32_e32 v59, 0x80, v49
	v_or_b32_e32 v60, v59, v1
	v_cndmask_b32_e64 v55, 0, 1, vcc
	v_cmp_ge_i32_e32 vcc, v53, v32
	v_min_i32_e32 v60, v60, v50
	v_or_b32_e32 v59, v59, v186
	v_addc_co_u32_e32 v54, vcc, v54, v55, vcc
	v_cmp_ge_i32_e32 vcc, v53, v33
	v_min_i32_e32 v50, v59, v50
	s_ashr_i32 s3, s2, 31
	v_cndmask_b32_e64 v55, 0, 1, vcc
	v_cmp_ge_i32_e32 vcc, v53, v38
	s_lshl_b64 s[0:1], s[2:3], 23
	s_add_u32 s5, s52, s0
	v_addc_co_u32_e32 v54, vcc, v54, v55, vcc
	v_cmp_ge_i32_e32 vcc, v53, v39
	s_addc_u32 s23, s53, s1
	s_lshl_b64 s[2:3], s[2:3], 15
	v_cndmask_b32_e64 v55, 0, 1, vcc
	v_cmp_ge_i32_e32 vcc, v53, v40
	s_add_u32 s2, s46, s2
	s_addc_u32 s3, s47, s3
	v_addc_co_u32_e32 v54, vcc, v54, v55, vcc
	v_cmp_ge_i32_e32 vcc, v53, v41
	s_lshl_b32 s64, s4, 8
	s_nop 0
	v_cndmask_b32_e64 v55, 0, 1, vcc
	v_cmp_ge_i32_e32 vcc, v53, v42
	s_nop 1
	v_addc_co_u32_e32 v54, vcc, v54, v55, vcc
	v_cmp_ge_i32_e32 vcc, v53, v43
	s_nop 1
	v_cndmask_b32_e64 v55, 0, 1, vcc
	v_cmp_ge_i32_e32 vcc, v53, v44
	s_nop 1
	v_addc_co_u32_e32 v54, vcc, v54, v55, vcc
	v_cmp_ge_i32_e32 vcc, v53, v45
	s_nop 1
	v_cndmask_b32_e64 v55, 0, 1, vcc
	v_cmp_ge_i32_e32 vcc, v53, v46
	s_nop 1
	v_addc_co_u32_e32 v54, vcc, v54, v55, vcc
	v_cmp_ge_i32_e32 vcc, v53, v47
	s_nop 1
	v_cndmask_b32_e64 v55, 0, 1, vcc
	v_cmp_ge_i32_e32 vcc, v53, v52
	s_nop 1
	v_addc_co_u32_e32 v54, vcc, v54, v55, vcc
	v_cmp_ge_i32_e32 vcc, v56, v30
	v_lshl_add_u32 v55, v54, 2, v51
	ds_read_b32 v55, v55
	v_cndmask_b32_e64 v57, 0, 1, vcc
	v_cmp_ge_i32_e32 vcc, v56, v31
	s_nop 1
	v_cndmask_b32_e64 v58, 0, 1, vcc
	v_cmp_ge_i32_e32 vcc, v56, v32
	s_nop 1
	v_addc_co_u32_e32 v57, vcc, v57, v58, vcc
	v_cmp_ge_i32_e32 vcc, v56, v33
	s_nop 1
	v_cndmask_b32_e64 v58, 0, 1, vcc
	v_cmp_ge_i32_e32 vcc, v56, v38
	s_nop 1
	v_addc_co_u32_e32 v57, vcc, v57, v58, vcc
	v_cmp_ge_i32_e32 vcc, v56, v39
	s_nop 1
	v_cndmask_b32_e64 v58, 0, 1, vcc
	v_cmp_ge_i32_e32 vcc, v56, v40
	s_nop 1
	v_addc_co_u32_e32 v57, vcc, v57, v58, vcc
	v_cmp_ge_i32_e32 vcc, v56, v41
	s_nop 1
	v_cndmask_b32_e64 v58, 0, 1, vcc
	v_cmp_ge_i32_e32 vcc, v56, v42
	s_nop 1
	v_addc_co_u32_e32 v57, vcc, v57, v58, vcc
	v_cmp_ge_i32_e32 vcc, v56, v43
	s_nop 1
	v_cndmask_b32_e64 v58, 0, 1, vcc
	v_cmp_ge_i32_e32 vcc, v56, v44
	s_nop 1
	v_addc_co_u32_e32 v57, vcc, v57, v58, vcc
	v_cmp_ge_i32_e32 vcc, v56, v45
	s_nop 1
	v_cndmask_b32_e64 v58, 0, 1, vcc
	v_cmp_ge_i32_e32 vcc, v56, v46
	s_nop 1
	v_addc_co_u32_e32 v57, vcc, v57, v58, vcc
	v_cmp_ge_i32_e32 vcc, v56, v47
	s_nop 1
	v_cndmask_b32_e64 v58, 0, 1, vcc
	v_cmp_ge_i32_e32 vcc, v56, v52
	s_nop 1
	v_addc_co_u32_e32 v57, vcc, v57, v58, vcc
	v_cmp_ge_i32_e32 vcc, v60, v30
	v_lshl_add_u32 v58, v57, 2, v51
	s_nop 0
	v_cndmask_b32_e64 v61, 0, 1, vcc
	v_cmp_ge_i32_e32 vcc, v60, v31
	s_nop 1
	v_cndmask_b32_e64 v62, 0, 1, vcc
	v_cmp_ge_i32_e32 vcc, v60, v32
	s_nop 1
	v_addc_co_u32_e32 v61, vcc, v61, v62, vcc
	v_cmp_ge_i32_e32 vcc, v60, v33
	s_nop 1
	v_cndmask_b32_e64 v62, 0, 1, vcc
	v_cmp_ge_i32_e32 vcc, v60, v38
	s_nop 1
	v_addc_co_u32_e32 v61, vcc, v61, v62, vcc
	v_cmp_ge_i32_e32 vcc, v60, v39
	s_nop 1
	v_cndmask_b32_e64 v62, 0, 1, vcc
	v_cmp_ge_i32_e32 vcc, v60, v40
	s_nop 1
	v_addc_co_u32_e32 v61, vcc, v61, v62, vcc
	v_cmp_ge_i32_e32 vcc, v60, v41
	s_nop 1
	v_cndmask_b32_e64 v62, 0, 1, vcc
	v_cmp_ge_i32_e32 vcc, v60, v42
	s_nop 1
	v_addc_co_u32_e32 v61, vcc, v61, v62, vcc
	v_cmp_ge_i32_e32 vcc, v60, v43
	s_nop 1
	v_cndmask_b32_e64 v62, 0, 1, vcc
	v_cmp_ge_i32_e32 vcc, v60, v44
	s_nop 1
	v_addc_co_u32_e32 v61, vcc, v61, v62, vcc
	v_cmp_ge_i32_e32 vcc, v60, v45
	s_nop 1
	v_cndmask_b32_e64 v62, 0, 1, vcc
	v_cmp_ge_i32_e32 vcc, v60, v46
	s_nop 1
	v_addc_co_u32_e32 v61, vcc, v61, v62, vcc
	v_cmp_ge_i32_e32 vcc, v60, v47
	s_nop 1
	v_cndmask_b32_e64 v62, 0, 1, vcc
	v_cmp_ge_i32_e32 vcc, v60, v52
	s_nop 1
	v_addc_co_u32_e32 v61, vcc, v61, v62, vcc
	v_cmp_ge_i32_e32 vcc, v50, v30
	v_lshl_add_u32 v62, v61, 2, v51
	s_nop 0
	v_cndmask_b32_e64 v30, 0, 1, vcc
	v_cmp_ge_i32_e32 vcc, v50, v31
	s_nop 1
	v_cndmask_b32_e64 v31, 0, 1, vcc
	v_cmp_ge_i32_e32 vcc, v50, v32
	s_nop 1
	v_addc_co_u32_e32 v30, vcc, v30, v31, vcc
	v_cmp_ge_i32_e32 vcc, v50, v33
	s_nop 1
	v_cndmask_b32_e64 v31, 0, 1, vcc
	v_cmp_ge_i32_e32 vcc, v50, v38
	s_nop 1
	v_addc_co_u32_e32 v30, vcc, v30, v31, vcc
	v_cmp_ge_i32_e32 vcc, v50, v39
	s_nop 1
	v_cndmask_b32_e64 v31, 0, 1, vcc
	v_cmp_ge_i32_e32 vcc, v50, v40
	s_nop 1
	v_addc_co_u32_e32 v30, vcc, v30, v31, vcc
	v_cmp_ge_i32_e32 vcc, v50, v41
	s_nop 1
	v_cndmask_b32_e64 v31, 0, 1, vcc
	v_cmp_ge_i32_e32 vcc, v50, v42
	s_nop 1
	v_addc_co_u32_e32 v30, vcc, v30, v31, vcc
	v_cmp_ge_i32_e32 vcc, v50, v43
	s_nop 1
	v_cndmask_b32_e64 v31, 0, 1, vcc
	v_cmp_ge_i32_e32 vcc, v50, v44
	s_nop 1
	v_addc_co_u32_e32 v30, vcc, v30, v31, vcc
	v_cmp_ge_i32_e32 vcc, v50, v45
	s_nop 1
	v_cndmask_b32_e64 v31, 0, 1, vcc
	v_cmp_ge_i32_e32 vcc, v50, v46
	s_nop 1
	v_addc_co_u32_e32 v30, vcc, v30, v31, vcc
	v_cmp_ge_i32_e32 vcc, v50, v47
	s_nop 1
	v_cndmask_b32_e64 v31, 0, 1, vcc
	v_cmp_ge_i32_e32 vcc, v50, v52
	s_nop 1
	v_addc_co_u32_e32 v40, vcc, v30, v31, vcc
	v_lshl_add_u32 v30, v40, 2, v51
	ds_read_b32 v32, v58
	ds_read_b32 v38, v62
	ds_read_b32 v41, v30
	s_waitcnt lgkmcnt(0)
	v_sub_u32_e32 v30, v53, v55
	v_lshl_add_u32 v30, v54, 9, v30
	v_sub_u32_e32 v32, v56, v32
	v_lshl_add_u32 v32, v57, 9, v32
	v_sub_u32_e32 v38, v60, v38
	v_lshl_add_u32 v40, v40, 9, v50
	v_ashrrev_i32_e32 v31, 31, v30
	v_ashrrev_i32_e32 v33, 31, v32
	v_lshl_add_u32 v38, v61, 9, v38
	v_sub_u32_e32 v40, v40, v41
	v_lshl_add_u64 v[30:31], v[30:31], 2, s[2:3]
	v_lshl_add_u64 v[32:33], v[32:33], 2, s[2:3]
	v_ashrrev_i32_e32 v39, 31, v38
	v_ashrrev_i32_e32 v41, 31, v40
	v_lshl_add_u64 v[38:39], v[38:39], 2, s[2:3]
	v_lshl_add_u64 v[40:41], v[40:41], 2, s[2:3]
	global_load_dword v30, v[30:31], off
	s_nop 0
	global_load_dword v31, v[32:33], off
	s_nop 0
	global_load_dword v32, v[38:39], off
	global_load_dword v33, v[40:41], off
	s_add_u32 s2, s26, s0
	s_addc_u32 s3, s27, s1
	s_lshl_b64 s[0:1], s[16:17], 9
	s_add_u32 s20, s2, s0
	v_sub_u32_e32 v38, v48, v49
	s_addc_u32 s21, s3, s1
	v_cmp_gt_i32_e32 vcc, s61, v38
	s_add_u32 s22, s5, s0
	s_addc_u32 s23, s23, s1
	v_cndmask_b32_e64 v208, 0, 1, vcc
	s_waitcnt vmcnt(0)
	v_lshl_or_b32 v209, v30, 12, v187
	v_lshl_or_b32 v210, v31, 12, v187
	v_lshl_or_b32 v211, v32, 12, v187
	v_lshl_or_b32 v212, v33, 12, v187

.LBB0_849:
	s_cmp_lt_i32 s76, s53
	s_cselect_b32 s61, s76, s60
	s_cmp_lt_i32 s61, 0
	s_cbranch_scc1 .LBB0_873
	s_add_u32 s62, s10, 0x1ed90000
	s_addc_u32 s63, s11, 0
	s_abs_i32 s64, s52
	v_cvt_f32_u32_e32 v4, s64
	s_sub_i32 s2, 0, s64
	s_abs_i32 s1, s61
	s_ashr_i32 s0, s61, 31
	v_rcp_iflag_f32_e32 v4, v4
	s_ashr_i32 s65, s52, 31
	s_lshr_b32 s9, s8, 6
	s_xor_b32 s0, s0, s65
	v_mul_f32_e32 v4, 0x4f7ffffe, v4
	v_cvt_u32_f32_e32 v4, v4
	v_lshlrev_b32_e32 v1, 4, v0
	v_and_b32_e32 v2, 32, v0
	v_bfe_u32 v3, v0, 2, 4
	v_readfirstlane_b32 s66, v4
	s_mul_i32 s2, s2, s66
	s_mul_hi_u32 s2, s66, s2
	s_add_i32 s66, s66, s2
	s_lshr_b32 s89, s61, 3
	s_lshl_b32 s89, s89, 2
	s_add_i32 s89, s89, 0x202e0
	v_mov_b32_e32 v222, s89
	ds_read_b32 v222, v222
	s_waitcnt lgkmcnt(0)
	v_lshlrev_b32_e32 v222, 2, v222
	v_add_u32_e32 v222, 0x20240, v222
	ds_read2_b32 v[252:253], v222 offset1:1
	s_waitcnt lgkmcnt(0)
	v_readfirstlane_b32 s90, v252
	v_readfirstlane_b32 s91, v253
	s_nop 3
	s_sub_i32 s91, s91, s90
	s_lshl_b32 s92, s90, 3
	s_sub_i32 s92, s61, s92
	s_and_b32 s18, s92, 7
	s_lshr_b32 s92, s92, 3
	s_add_i32 s3, s90, s92
	s_lshl_b32 s0, s3, 2
	s_add_i32 s0, s0, 0
	s_add_i32 s0, s0, 0x202e0
	v_mov_b32_e32 v4, s0
	ds_read_b32 v4, v4
	v_bitop3_b32 v1, v1, v2, 48 bitop3:0x6c
	v_lshrrev_b32_e32 v2, 3, v0
	s_lshl_b32 s20, s3, 8
	v_and_or_b32 v5, v2, 48, v3
	v_or_b32_e32 v2, 64, v2
	s_movk_i32 s0, 0x70
	s_ashr_i32 s21, s20, 31
	v_and_or_b32 v2, v2, s0, v3
	s_waitcnt lgkmcnt(0)
	v_lshlrev_b32_e32 v3, 2, v4
	s_lshl_b64 s[0:1], s[20:21], 11
	v_add_u32_e32 v3, 0, v3
	s_add_u32 s22, s62, s0
	v_add_u32_e32 v6, 0x20240, v3
	v_add_u32_e32 v3, 0x201c0, v3
	s_addc_u32 s23, s63, s1
	s_lshl_b32 s0, s9, 10
	v_and_or_b32 v1, v0, 64, v1
	ds_read_b32 v6, v6
	ds_read_b32 v3, v3
	s_add_i32 s21, s0, 0
	s_waitcnt vmcnt(0)
	s_add_i32 s67, s21, 0x2000
	v_lshl_or_b32 v180, v5, 11, v1
	s_waitcnt lgkmcnt(0)
	s_barrier
	s_mov_b32 m0, s21
	v_lshl_or_b32 v182, v2, 11, v1
	global_load_lds_dwordx4 v180, s[22:23]
	s_mov_b32 m0, s67
	s_waitcnt lgkmcnt(0)
	v_subrev_u32_e32 v1, s3, v6
	global_load_lds_dwordx4 v182, s[22:23]
	v_lshlrev_b32_e32 v1, 8, v1
	v_add_u32_e32 v1, v1, v3
	s_movk_i32 s3, 0x80
	s_movk_i32 s0, 0x81
	v_cmp_lt_i32_e32 vcc, s3, v1
	v_mov_b32_e32 v187, 0
	v_readfirstlane_b32 s2, v4
	v_cmp_gt_i32_e64 s[0:1], s0, v1
	v_or_b32_e32 v184, 0x40000, v180
	v_or_b32_e32 v186, 0x40000, v182
	v_mov_b32_e32 v185, v187
	s_cbranch_vccz .LBB0_852
	s_add_i32 m0, s21, 0x4000
	v_lshl_add_u64 v[2:3], s[22:23], 0, v[186:187]
	global_load_lds_dwordx4 v184, s[22:23]
	s_add_i32 m0, s21, 0x6000
	s_nop 0
	global_load_lds_dwordx4 v[2:3], off

.LBB0_853:
	s_add_i32 s0, s61, s33
	s_cmp_lt_i32 s61, s53
	s_cselect_b32 s1, s60, -1
	s_cmp_lt_i32 s0, s53
	s_cselect_b32 s61, s0, s1
	s_cmp_lt_i32 s61, 0
	s_cselect_b64 s[24:25], -1, 0
	s_and_b64 vcc, exec, s[24:25]
	s_mov_b32 s36, s18
	s_mov_b32 s42, s20
	s_cbranch_vccnz .LBB0_855
	s_lshr_b32 s89, s61, 3
	s_lshl_b32 s89, s89, 2
	s_add_i32 s89, s89, 0x202e0
	v_mov_b32_e32 v222, s89
	ds_read_b32 v222, v222
	s_waitcnt lgkmcnt(0)
	v_lshlrev_b32_e32 v222, 2, v222
	v_add_u32_e32 v222, 0x20240, v222
	ds_read2_b32 v[252:253], v222 offset1:1
	s_waitcnt lgkmcnt(0)
	v_readfirstlane_b32 s90, v252
	v_readfirstlane_b32 s91, v253
	s_nop 3
	s_sub_i32 s91, s91, s90
	s_lshl_b32 s92, s90, 3
	s_sub_i32 s92, s61, s92
	s_and_b32 s36, s92, 7
	s_lshr_b32 s92, s92, 3
	s_add_i32 s2, s90, s92
	s_lshl_b32 s0, s2, 2
	s_add_i32 s0, s0, 0
	s_add_i32 s0, s0, 0x202e0
	v_mov_b32_e32 v1, s0
	ds_read_b32 v1, v1
	s_ashr_i32 s37, s36, 31
	s_waitcnt lgkmcnt(0)
	v_lshlrev_b32_e32 v2, 2, v1
	v_add_u32_e32 v2, 0, v2
	v_readfirstlane_b32 s0, v1
	v_add_u32_e32 v3, 0x20240, v2
	s_ashr_i32 s1, s0, 31
	ds_read_b32 v3, v3
	s_lshl_b64 s[0:1], s[0:1], 23
	v_add_u32_e32 v2, 0x201c0, v2
	s_add_u32 s3, s54, s0
	ds_read_b32 v2, v2
	s_addc_u32 s27, s55, s1
	s_lshl_b32 s42, s2, 8
	s_lshl_b64 s[0:1], s[36:37], 10
	s_add_u32 s26, s3, s0
	s_addc_u32 s27, s27, s1
	s_waitcnt lgkmcnt(0)
	v_subrev_u32_e32 v1, s2, v3
	s_add_u32 s38, s26, 0x200
	v_lshlrev_b32_e32 v1, 8, v1
	s_addc_u32 s39, s27, 0
	s_ashr_i32 s43, s42, 31
	v_add_u32_e32 v1, v1, v2
	s_lshl_b64 s[0:1], s[42:43], 11
	v_cmp_gt_i32_e32 vcc, s19, v1
	s_add_u32 s40, s62, s0
	s_addc_u32 s41, s63, s1
	v_cndmask_b32_e64 v208, 0, 1, vcc
